# baseline (speedup 1.0000x reference)
.Lg2_qk_epi:
	s_lshr_b32 s95, s50, 12
	s_lshl_b32 s95, s95, 9
	s_lshr_b32 s96, s94, 2
	s_add_u32 s95, s95, s96
	s_lshl_b32 s95, s95, 14
	s_add_u32 s96, s18, s95
	s_addc_u32 s97, s19, 0
	v_lshrrev_b32_e32 v200, 8, v0
	v_bfe_u32 v201, v0, 4, 2
	v_lshlrev_b32_e32 v200, 5, v200
	v_lshl_add_u32 v200, v201, 1, v200
	v_lshlrev_b32_e32 v200, 14, v200
	v_and_b32_e32 v202, 15, v0
	v_lshrrev_b32_e32 v201, 1, v0
	v_and_b32_e32 v201, 0x60, v201
	v_or3_b32 v202, v201, v202, s50
	v_and_b32_e32 v202, 0xfff, v202
	v_lshl_add_u32 v203, v202, 2, v200
	v_mov_b32_e32 v204, v203
	v_add_u32_e32 v205, 0x4000, v203
	v_add_u32_e32 v206, 0x20000, v203
	v_add_u32_e32 v207, 0x24000, v203
	v_add_u32_e32 v208, 0x40000, v203
	v_add_u32_e32 v209, 0x44000, v203
	v_add_u32_e32 v210, 0x60000, v203
	v_add_u32_e32 v211, 0x64000, v203
	s_mov_b32 s92, 0x3a800000
	s_mov_b32 s93, 0x3a800000
	v_pk_fma_f32 v[126:127], v[126:127], s[92:93], v[158:159]
	v_pk_fma_f32 v[128:129], v[128:129], s[92:93], v[160:161]
	v_pk_fma_f32 v[62:63], v[62:63], s[92:93], v[142:143]
	v_pk_fma_f32 v[64:65], v[64:65], s[92:93], v[144:145]
	v_cvt_pk_fp8_f32 v212, v126, v127
	v_cvt_pk_fp8_f32 v213, v128, v129
	v_cvt_pk_fp8_f32 v212, v62, v63 op_sel:[0,0,1]
	v_cvt_pk_fp8_f32 v213, v64, v65 op_sel:[0,0,1]
	v_pk_fma_f32 v[122:123], v[122:123], s[92:93], v[158:159]
	v_pk_fma_f32 v[124:125], v[124:125], s[92:93], v[160:161]
	v_pk_fma_f32 v[54:55], v[54:55], s[92:93], v[142:143]
	v_pk_fma_f32 v[56:57], v[56:57], s[92:93], v[144:145]
	global_store_dword v204, v212, s[96:97]
	global_store_dword v205, v213, s[96:97]
	v_cvt_pk_fp8_f32 v214, v122, v123
	v_cvt_pk_fp8_f32 v215, v124, v125
	v_cvt_pk_fp8_f32 v214, v54, v55 op_sel:[0,0,1]
	v_cvt_pk_fp8_f32 v215, v56, v57 op_sel:[0,0,1]
	v_pk_fma_f32 v[118:119], v[118:119], s[92:93], v[158:159]
	v_pk_fma_f32 v[120:121], v[120:121], s[92:93], v[160:161]
	v_pk_fma_f32 v[70:71], v[70:71], s[92:93], v[142:143]
	v_pk_fma_f32 v[72:73], v[72:73], s[92:93], v[144:145]
	global_store_dword v204, v214, s[96:97] offset:64
	global_store_dword v205, v215, s[96:97] offset:64
	v_cvt_pk_fp8_f32 v216, v118, v119
	v_cvt_pk_fp8_f32 v217, v120, v121
	v_cvt_pk_fp8_f32 v216, v70, v71 op_sel:[0,0,1]
	v_cvt_pk_fp8_f32 v217, v72, v73 op_sel:[0,0,1]
	v_pk_fma_f32 v[114:115], v[114:115], s[92:93], v[158:159]
	v_pk_fma_f32 v[116:117], v[116:117], s[92:93], v[160:161]
	v_pk_fma_f32 v[58:59], v[58:59], s[92:93], v[142:143]
	v_pk_fma_f32 v[60:61], v[60:61], s[92:93], v[144:145]
	global_store_dword v204, v216, s[96:97] offset:512
	global_store_dword v205, v217, s[96:97] offset:512
	v_cvt_pk_fp8_f32 v218, v114, v115
	v_cvt_pk_fp8_f32 v219, v116, v117
	v_cvt_pk_fp8_f32 v218, v58, v59 op_sel:[0,0,1]
	v_cvt_pk_fp8_f32 v219, v60, v61 op_sel:[0,0,1]
	v_pk_fma_f32 v[110:111], v[110:111], s[92:93], v[154:155]
	v_pk_fma_f32 v[112:113], v[112:113], s[92:93], v[156:157]
	v_pk_fma_f32 v[42:43], v[42:43], s[92:93], v[138:139]
	v_pk_fma_f32 v[44:45], v[44:45], s[92:93], v[140:141]
	global_store_dword v204, v218, s[96:97] offset:576
	global_store_dword v205, v219, s[96:97] offset:576
	v_cvt_pk_fp8_f32 v220, v110, v111
	v_cvt_pk_fp8_f32 v221, v112, v113
	v_cvt_pk_fp8_f32 v220, v42, v43 op_sel:[0,0,1]
	v_cvt_pk_fp8_f32 v221, v44, v45 op_sel:[0,0,1]
	v_pk_fma_f32 v[98:99], v[98:99], s[92:93], v[154:155]
	v_pk_fma_f32 v[100:101], v[100:101], s[92:93], v[156:157]
	v_pk_fma_f32 v[34:35], v[34:35], s[92:93], v[138:139]
	v_pk_fma_f32 v[36:37], v[36:37], s[92:93], v[140:141]
	global_store_dword v206, v220, s[96:97]
	global_store_dword v207, v221, s[96:97]
	v_cvt_pk_fp8_f32 v222, v98, v99
	v_cvt_pk_fp8_f32 v223, v100, v101
	v_cvt_pk_fp8_f32 v222, v34, v35 op_sel:[0,0,1]
	v_cvt_pk_fp8_f32 v223, v36, v37 op_sel:[0,0,1]
	v_pk_fma_f32 v[106:107], v[106:107], s[92:93], v[154:155]
	v_pk_fma_f32 v[108:109], v[108:109], s[92:93], v[156:157]
	v_pk_fma_f32 v[46:47], v[46:47], s[92:93], v[138:139]
	v_pk_fma_f32 v[48:49], v[48:49], s[92:93], v[140:141]
	global_store_dword v206, v222, s[96:97] offset:64
	global_store_dword v207, v223, s[96:97] offset:64
	v_cvt_pk_fp8_f32 v224, v106, v107
	v_cvt_pk_fp8_f32 v225, v108, v109
	v_cvt_pk_fp8_f32 v224, v46, v47 op_sel:[0,0,1]
	v_cvt_pk_fp8_f32 v225, v48, v49 op_sel:[0,0,1]
	v_pk_fma_f32 v[102:103], v[102:103], s[92:93], v[154:155]
	v_pk_fma_f32 v[104:105], v[104:105], s[92:93], v[156:157]
	v_pk_fma_f32 v[38:39], v[38:39], s[92:93], v[138:139]
	v_pk_fma_f32 v[40:41], v[40:41], s[92:93], v[140:141]
	global_store_dword v206, v224, s[96:97] offset:512
	global_store_dword v207, v225, s[96:97] offset:512
	v_cvt_pk_fp8_f32 v226, v102, v103
	v_cvt_pk_fp8_f32 v227, v104, v105
	v_cvt_pk_fp8_f32 v226, v38, v39 op_sel:[0,0,1]
	v_cvt_pk_fp8_f32 v227, v40, v41 op_sel:[0,0,1]
	v_pk_fma_f32 v[86:87], v[86:87], s[92:93], v[150:151]
	v_pk_fma_f32 v[88:89], v[88:89], s[92:93], v[152:153]
	v_pk_fma_f32 v[26:27], v[26:27], s[92:93], v[134:135]
	v_pk_fma_f32 v[28:29], v[28:29], s[92:93], v[136:137]
	global_store_dword v206, v226, s[96:97] offset:576
	global_store_dword v207, v227, s[96:97] offset:576
	v_cvt_pk_fp8_f32 v228, v86, v87
	v_cvt_pk_fp8_f32 v229, v88, v89
	v_cvt_pk_fp8_f32 v228, v26, v27 op_sel:[0,0,1]
	v_cvt_pk_fp8_f32 v229, v28, v29 op_sel:[0,0,1]
	v_pk_fma_f32 v[82:83], v[82:83], s[92:93], v[150:151]
	v_pk_fma_f32 v[84:85], v[84:85], s[92:93], v[152:153]
	v_pk_fma_f32 v[18:19], v[18:19], s[92:93], v[134:135]
	v_pk_fma_f32 v[20:21], v[20:21], s[92:93], v[136:137]
	global_store_dword v208, v228, s[96:97]
	global_store_dword v209, v229, s[96:97]
	v_cvt_pk_fp8_f32 v230, v82, v83
	v_cvt_pk_fp8_f32 v231, v84, v85
	v_cvt_pk_fp8_f32 v230, v18, v19 op_sel:[0,0,1]
	v_cvt_pk_fp8_f32 v231, v20, v21 op_sel:[0,0,1]
	v_pk_fma_f32 v[94:95], v[94:95], s[92:93], v[150:151]
	v_pk_fma_f32 v[96:97], v[96:97], s[92:93], v[152:153]
	v_pk_fma_f32 v[30:31], v[30:31], s[92:93], v[134:135]
	v_pk_fma_f32 v[32:33], v[32:33], s[92:93], v[136:137]
	global_store_dword v208, v230, s[96:97] offset:64
	global_store_dword v209, v231, s[96:97] offset:64
	v_cvt_pk_fp8_f32 v232, v94, v95
	v_cvt_pk_fp8_f32 v233, v96, v97
	v_cvt_pk_fp8_f32 v232, v30, v31 op_sel:[0,0,1]
	v_cvt_pk_fp8_f32 v233, v32, v33 op_sel:[0,0,1]
	v_pk_fma_f32 v[90:91], v[90:91], s[92:93], v[150:151]
	v_pk_fma_f32 v[92:93], v[92:93], s[92:93], v[152:153]
	v_pk_fma_f32 v[22:23], v[22:23], s[92:93], v[134:135]
	v_pk_fma_f32 v[24:25], v[24:25], s[92:93], v[136:137]
	global_store_dword v208, v232, s[96:97] offset:512
	global_store_dword v209, v233, s[96:97] offset:512
	v_cvt_pk_fp8_f32 v234, v90, v91
	v_cvt_pk_fp8_f32 v235, v92, v93
	v_cvt_pk_fp8_f32 v234, v22, v23 op_sel:[0,0,1]
	v_cvt_pk_fp8_f32 v235, v24, v25 op_sel:[0,0,1]
	v_pk_fma_f32 v[66:67], v[66:67], s[92:93], v[146:147]
	v_pk_fma_f32 v[68:69], v[68:69], s[92:93], v[148:149]
	v_pk_fma_f32 v[10:11], v[10:11], s[92:93], v[130:131]
	v_pk_fma_f32 v[12:13], v[12:13], s[92:93], v[132:133]
	global_store_dword v208, v234, s[96:97] offset:576
	global_store_dword v209, v235, s[96:97] offset:576
	v_cvt_pk_fp8_f32 v236, v66, v67
	v_cvt_pk_fp8_f32 v237, v68, v69
	v_cvt_pk_fp8_f32 v236, v10, v11 op_sel:[0,0,1]
	v_cvt_pk_fp8_f32 v237, v12, v13 op_sel:[0,0,1]
	v_pk_fma_f32 v[50:51], v[50:51], s[92:93], v[146:147]
	v_pk_fma_f32 v[52:53], v[52:53], s[92:93], v[148:149]
	v_pk_fma_f32 v[2:3], v[2:3], s[92:93], v[130:131]
	v_pk_fma_f32 v[4:5], v[4:5], s[92:93], v[132:133]
	global_store_dword v210, v236, s[96:97]
	global_store_dword v211, v237, s[96:97]
	v_cvt_pk_fp8_f32 v238, v50, v51
	v_cvt_pk_fp8_f32 v239, v52, v53
	v_cvt_pk_fp8_f32 v238, v2, v3 op_sel:[0,0,1]
	v_cvt_pk_fp8_f32 v239, v4, v5 op_sel:[0,0,1]
	v_pk_fma_f32 v[78:79], v[78:79], s[92:93], v[146:147]
	v_pk_fma_f32 v[80:81], v[80:81], s[92:93], v[148:149]
	v_pk_fma_f32 v[14:15], v[14:15], s[92:93], v[130:131]
	v_pk_fma_f32 v[16:17], v[16:17], s[92:93], v[132:133]
	global_store_dword v210, v238, s[96:97] offset:64
	global_store_dword v211, v239, s[96:97] offset:64
	v_cvt_pk_fp8_f32 v240, v78, v79
	v_cvt_pk_fp8_f32 v241, v80, v81
	v_cvt_pk_fp8_f32 v240, v14, v15 op_sel:[0,0,1]
	v_cvt_pk_fp8_f32 v241, v16, v17 op_sel:[0,0,1]
	v_pk_fma_f32 v[74:75], v[74:75], s[92:93], v[146:147]
	v_pk_fma_f32 v[76:77], v[76:77], s[92:93], v[148:149]
	v_pk_fma_f32 v[6:7], v[6:7], s[92:93], v[130:131]
	v_pk_fma_f32 v[8:9], v[8:9], s[92:93], v[132:133]
	global_store_dword v210, v240, s[96:97] offset:512
	global_store_dword v211, v241, s[96:97] offset:512
	v_cvt_pk_fp8_f32 v242, v74, v75
	v_cvt_pk_fp8_f32 v243, v76, v77
	v_cvt_pk_fp8_f32 v242, v6, v7 op_sel:[0,0,1]
	v_cvt_pk_fp8_f32 v243, v8, v9 op_sel:[0,0,1]
	s_nop 1
	global_store_dword v210, v242, s[96:97] offset:576
	global_store_dword v211, v243, s[96:97] offset:576
	s_mov_b64 s[56:57], 0
	s_andn2_b64 vcc, exec, s[52:53]
	s_mov_b32 s50, s54
	s_cbranch_vccz .LBB2_26
	s_branch .LBB2_8
.LBB2_26:
	s_endpgm
	s_nop 0
	s_nop 0
	s_nop 0
	s_nop 0
	s_nop 0
	s_nop 0
	s_nop 0
	s_nop 0
	s_nop 0
	s_nop 0
	s_nop 0
	s_nop 0
	s_nop 0
	s_nop 0
	s_nop 0
	s_nop 0
	s_nop 0
	s_nop 0
	s_nop 0
	s_nop 0
	s_nop 0
	s_nop 0
	s_nop 0
	s_nop 0
	s_nop 0
	s_nop 0
	s_nop 0
	s_nop 0
	s_nop 0
	s_nop 0
	s_nop 0
	s_nop 0
	s_nop 0
	s_nop 0
	s_nop 0
	s_nop 0
	s_nop 0
	s_nop 0
	s_nop 0
	s_nop 0
	s_nop 0
	s_nop 0
	s_nop 0
	s_nop 0
	s_nop 0
	s_nop 0
	s_nop 0
	s_nop 0
	s_nop 0
	s_nop 0
	s_nop 0
	s_nop 0
	s_endpgm
